# v54 + top-k threshold search exits as soon as a ballot step counts exactly 16 keys (the selected set is then final; identical result)
# speedup vs baseline: 1.0166x; 1.0120x over previous
.LBB0_1701:
	s_or_b64 exec, exec, s[4:5]
	v_cndmask_b32_e64 v0, v1, v171, s[10:11]
	v_cndmask_b32_e32 v5, v0, v169, vcc
	v_not_b32_e32 v0, v5
	v_or_b32_e32 v1, 0x80000000, v5
	v_cmp_gt_i32_e64 s[18:19], 0, v5
	s_nop 1
	v_cndmask_b32_e64 v2, v1, v0, s[18:19]
	v_cmp_gt_i32_e64 s[18:19], 0, v2
	s_bcnt1_i32_b64 s1, s[18:19]
	s_mov_b32 s7, 0
	s_cmp_gt_i32 s1, 15
	v_lshlrev_b64 v[0:1], 6, v[2:3]
	s_cselect_b32 s1, 32, 0
	v_or_b32_e32 v0, v0, v146
	s_or_b32 s91, s1, 16
	v_cmp_le_u64_e64 s[18:19], s[90:91], v[0:1]
	s_bcnt1_i32_b64 s4, s[18:19]
	s_cmp_gt_i32 s4, 15
	s_cselect_b32 s1, s91, s1
	s_cmp_eq_u32 s4, 16
	s_cbranch_scc1 .Ltopk_exit
	s_or_b32 s91, s1, 8
	v_cmp_le_u64_e64 s[18:19], s[90:91], v[0:1]
	s_bcnt1_i32_b64 s4, s[18:19]
	s_cmp_gt_i32 s4, 15
	s_cselect_b32 s1, s91, s1
	s_cmp_eq_u32 s4, 16
	s_cbranch_scc1 .Ltopk_exit
	s_or_b32 s91, s1, 4
	v_cmp_le_u64_e64 s[18:19], s[90:91], v[0:1]
	s_bcnt1_i32_b64 s4, s[18:19]
	s_cmp_gt_i32 s4, 15
	s_cselect_b32 s1, s91, s1
	s_cmp_eq_u32 s4, 16
	s_cbranch_scc1 .Ltopk_exit
	s_or_b32 s91, s1, 2
	v_cmp_le_u64_e64 s[18:19], s[90:91], v[0:1]
	s_bcnt1_i32_b64 s4, s[18:19]
	s_cmp_gt_i32 s4, 15
	s_cselect_b32 s1, s91, s1
	s_cmp_eq_u32 s4, 16
	s_cbranch_scc1 .Ltopk_exit
	s_or_b32 s91, s1, 1
	v_cmp_le_u64_e64 s[18:19], s[90:91], v[0:1]
	s_bcnt1_i32_b64 s4, s[18:19]
	s_cmp_gt_i32 s4, 15
	s_cselect_b32 s1, s91, s1
	s_cmp_eq_u32 s4, 16
	s_cbranch_scc1 .Ltopk_exit
	v_cmp_le_u64_e64 s[18:19], s[0:1], v[0:1]
	s_bcnt1_i32_b64 s4, s[18:19]
	s_cmp_gt_i32 s4, 15
	s_cselect_b32 s7, 0x80000000, 0
	s_cmp_eq_u32 s4, 16
	s_cbranch_scc1 .Ltopk_exit
	s_or_b32 s4, s7, 2.0
	s_mov_b32 s5, s1
	v_cmp_le_u64_e64 s[18:19], s[4:5], v[0:1]
	s_bcnt1_i32_b64 s5, s[18:19]
	s_cmp_gt_i32 s5, 15
	s_cselect_b32 s7, s4, s7
	s_cmp_eq_u32 s5, 16
	s_cbranch_scc1 .Ltopk_exit
	s_or_b32 s4, s7, 0x20000000
	s_mov_b32 s5, s1
	v_cmp_le_u64_e64 s[18:19], s[4:5], v[0:1]
	s_bcnt1_i32_b64 s5, s[18:19]
	s_cmp_gt_i32 s5, 15
	s_cselect_b32 s7, s4, s7
	s_cmp_eq_u32 s5, 16
	s_cbranch_scc1 .Ltopk_exit
	s_or_b32 s4, s7, 0x10000000
	s_mov_b32 s5, s1
	v_cmp_le_u64_e64 s[18:19], s[4:5], v[0:1]
	s_bcnt1_i32_b64 s5, s[18:19]
	s_cmp_gt_i32 s5, 15
	s_cselect_b32 s7, s4, s7
	s_cmp_eq_u32 s5, 16
	s_cbranch_scc1 .Ltopk_exit
	s_or_b32 s4, s7, 0x8000000
	s_mov_b32 s5, s1
	v_cmp_le_u64_e64 s[18:19], s[4:5], v[0:1]
	s_bcnt1_i32_b64 s5, s[18:19]
	s_cmp_gt_i32 s5, 15
	s_cselect_b32 s7, s4, s7
	s_cmp_eq_u32 s5, 16
	s_cbranch_scc1 .Ltopk_exit
	s_or_b32 s4, s7, 0x4000000
	s_mov_b32 s5, s1
	v_cmp_le_u64_e64 s[18:19], s[4:5], v[0:1]
	s_bcnt1_i32_b64 s5, s[18:19]
	s_cmp_gt_i32 s5, 15
	s_cselect_b32 s7, s4, s7
	s_cmp_eq_u32 s5, 16
	s_cbranch_scc1 .Ltopk_exit
	s_or_b32 s4, s7, 0x2000000
	s_mov_b32 s5, s1
	v_cmp_le_u64_e64 s[18:19], s[4:5], v[0:1]
	s_bcnt1_i32_b64 s5, s[18:19]
	s_cmp_gt_i32 s5, 15
	s_cselect_b32 s7, s4, s7
	s_cmp_eq_u32 s5, 16
	s_cbranch_scc1 .Ltopk_exit
	s_or_b32 s4, s7, 0x1000000
	s_mov_b32 s5, s1
	v_cmp_le_u64_e64 s[18:19], s[4:5], v[0:1]
	s_bcnt1_i32_b64 s5, s[18:19]
	s_cmp_gt_i32 s5, 15
	s_cselect_b32 s7, s4, s7
	s_cmp_eq_u32 s5, 16
	s_cbranch_scc1 .Ltopk_exit
	s_or_b32 s4, s7, 0x800000
	s_mov_b32 s5, s1
	v_cmp_le_u64_e64 s[18:19], s[4:5], v[0:1]
	s_bcnt1_i32_b64 s5, s[18:19]
	s_cmp_gt_i32 s5, 15
	s_cselect_b32 s7, s4, s7
	s_cmp_eq_u32 s5, 16
	s_cbranch_scc1 .Ltopk_exit
	s_or_b32 s4, s7, 0x400000
	s_mov_b32 s5, s1
	v_cmp_le_u64_e64 s[18:19], s[4:5], v[0:1]
	s_bcnt1_i32_b64 s5, s[18:19]
	s_cmp_gt_i32 s5, 15
	s_cselect_b32 s7, s4, s7
	s_cmp_eq_u32 s5, 16
	s_cbranch_scc1 .Ltopk_exit
	s_or_b32 s4, s7, 0x200000
	s_mov_b32 s5, s1
	v_cmp_le_u64_e64 s[18:19], s[4:5], v[0:1]
	s_bcnt1_i32_b64 s5, s[18:19]
	s_cmp_gt_i32 s5, 15
	s_cselect_b32 s7, s4, s7
	s_cmp_eq_u32 s5, 16
	s_cbranch_scc1 .Ltopk_exit
	s_or_b32 s4, s7, 0x100000
	s_mov_b32 s5, s1
	v_cmp_le_u64_e64 s[18:19], s[4:5], v[0:1]
	s_bcnt1_i32_b64 s5, s[18:19]
	s_cmp_gt_i32 s5, 15
	s_cselect_b32 s7, s4, s7
	s_cmp_eq_u32 s5, 16
	s_cbranch_scc1 .Ltopk_exit
	s_or_b32 s4, s7, 0x80000
	s_mov_b32 s5, s1
	v_cmp_le_u64_e64 s[18:19], s[4:5], v[0:1]
	s_bcnt1_i32_b64 s5, s[18:19]
	s_cmp_gt_i32 s5, 15
	s_cselect_b32 s7, s4, s7
	s_cmp_eq_u32 s5, 16
	s_cbranch_scc1 .Ltopk_exit
	s_or_b32 s4, s7, 0x40000
	s_mov_b32 s5, s1
	v_cmp_le_u64_e64 s[18:19], s[4:5], v[0:1]
	s_bcnt1_i32_b64 s5, s[18:19]
	s_cmp_gt_i32 s5, 15
	s_cselect_b32 s7, s4, s7
	s_cmp_eq_u32 s5, 16
	s_cbranch_scc1 .Ltopk_exit
	s_or_b32 s4, s7, 0x20000
	s_mov_b32 s5, s1
	v_cmp_le_u64_e64 s[18:19], s[4:5], v[0:1]
	s_bcnt1_i32_b64 s5, s[18:19]
	s_cmp_gt_i32 s5, 15
	s_cselect_b32 s7, s4, s7
	s_cmp_eq_u32 s5, 16
	s_cbranch_scc1 .Ltopk_exit
	s_or_b32 s4, s7, 0x10000
	s_mov_b32 s5, s1
	v_cmp_le_u64_e64 s[18:19], s[4:5], v[0:1]
	s_bcnt1_i32_b64 s5, s[18:19]
	s_cmp_gt_i32 s5, 15
	s_cselect_b32 s7, s4, s7
	s_cmp_eq_u32 s5, 16
	s_cbranch_scc1 .Ltopk_exit
	s_or_b32 s4, s7, 0x8000
	s_mov_b32 s5, s1
	v_cmp_le_u64_e64 s[18:19], s[4:5], v[0:1]
	s_bcnt1_i32_b64 s5, s[18:19]
	s_cmp_gt_i32 s5, 15
	s_cselect_b32 s7, s4, s7
	s_cmp_eq_u32 s5, 16
	s_cbranch_scc1 .Ltopk_exit
	s_or_b32 s4, s7, 0x4000
	s_mov_b32 s5, s1
	v_cmp_le_u64_e64 s[18:19], s[4:5], v[0:1]
	s_bcnt1_i32_b64 s5, s[18:19]
	s_cmp_gt_i32 s5, 15
	s_cselect_b32 s7, s4, s7
	s_cmp_eq_u32 s5, 16
	s_cbranch_scc1 .Ltopk_exit
	s_or_b32 s4, s7, 0x2000
	s_mov_b32 s5, s1
	v_cmp_le_u64_e64 s[18:19], s[4:5], v[0:1]
	s_bcnt1_i32_b64 s5, s[18:19]
	s_cmp_gt_i32 s5, 15
	s_cselect_b32 s7, s4, s7
	s_cmp_eq_u32 s5, 16
	s_cbranch_scc1 .Ltopk_exit
	s_or_b32 s4, s7, 0x1000
	s_mov_b32 s5, s1
	v_cmp_le_u64_e64 s[18:19], s[4:5], v[0:1]
	s_bcnt1_i32_b64 s5, s[18:19]
	s_cmp_gt_i32 s5, 15
	s_cselect_b32 s7, s4, s7
	s_cmp_eq_u32 s5, 16
	s_cbranch_scc1 .Ltopk_exit
	s_or_b32 s4, s7, 0x800
	s_mov_b32 s5, s1
	v_cmp_le_u64_e64 s[18:19], s[4:5], v[0:1]
	s_bcnt1_i32_b64 s5, s[18:19]
	s_cmp_gt_i32 s5, 15
	s_cselect_b32 s7, s4, s7
	s_cmp_eq_u32 s5, 16
	s_cbranch_scc1 .Ltopk_exit
	s_or_b32 s4, s7, 0x400
	s_mov_b32 s5, s1
	v_cmp_le_u64_e64 s[18:19], s[4:5], v[0:1]
	s_bcnt1_i32_b64 s5, s[18:19]
	s_cmp_gt_i32 s5, 15
	s_cselect_b32 s7, s4, s7
	s_cmp_eq_u32 s5, 16
	s_cbranch_scc1 .Ltopk_exit
	s_or_b32 s4, s7, 0x200
	s_mov_b32 s5, s1
	v_cmp_le_u64_e64 s[18:19], s[4:5], v[0:1]
	s_bcnt1_i32_b64 s5, s[18:19]
	s_cmp_gt_i32 s5, 15
	s_cselect_b32 s7, s4, s7
	s_cmp_eq_u32 s5, 16
	s_cbranch_scc1 .Ltopk_exit
	s_or_b32 s4, s7, 0x100
	s_mov_b32 s5, s1
	v_cmp_le_u64_e64 s[18:19], s[4:5], v[0:1]
	s_bcnt1_i32_b64 s5, s[18:19]
	s_cmp_gt_i32 s5, 15
	s_cselect_b32 s7, s4, s7
	s_cmp_eq_u32 s5, 16
	s_cbranch_scc1 .Ltopk_exit
	s_or_b32 s4, s7, 0x80
	s_mov_b32 s5, s1
	v_cmp_le_u64_e64 s[18:19], s[4:5], v[0:1]
	s_bcnt1_i32_b64 s5, s[18:19]
	s_cmp_gt_i32 s5, 15
	s_cselect_b32 s7, s4, s7
	s_cmp_eq_u32 s5, 16
	s_cbranch_scc1 .Ltopk_exit
	s_or_b32 s4, s7, 64
	s_mov_b32 s5, s1
	v_cmp_le_u64_e64 s[18:19], s[4:5], v[0:1]
	s_bcnt1_i32_b64 s5, s[18:19]
	s_cmp_gt_i32 s5, 15
	s_cselect_b32 s7, s4, s7
	s_cmp_eq_u32 s5, 16
	s_cbranch_scc1 .Ltopk_exit
	s_or_b32 s4, s7, 32
	s_mov_b32 s5, s1
	v_cmp_le_u64_e64 s[18:19], s[4:5], v[0:1]
	s_bcnt1_i32_b64 s5, s[18:19]
	s_cmp_gt_i32 s5, 15
	s_cselect_b32 s7, s4, s7
	s_cmp_eq_u32 s5, 16
	s_cbranch_scc1 .Ltopk_exit
	s_or_b32 s4, s7, 16
	s_mov_b32 s5, s1
	v_cmp_le_u64_e64 s[18:19], s[4:5], v[0:1]
	s_bcnt1_i32_b64 s5, s[18:19]
	s_cmp_gt_i32 s5, 15
	s_cselect_b32 s7, s4, s7
	s_cmp_eq_u32 s5, 16
	s_cbranch_scc1 .Ltopk_exit
	s_or_b32 s4, s7, 8
	s_mov_b32 s5, s1
	v_cmp_le_u64_e64 s[18:19], s[4:5], v[0:1]
	s_bcnt1_i32_b64 s5, s[18:19]
	s_cmp_gt_i32 s5, 15
	s_cselect_b32 s7, s4, s7
	s_cmp_eq_u32 s5, 16
	s_cbranch_scc1 .Ltopk_exit
	s_or_b32 s4, s7, 4
	s_mov_b32 s5, s1
	v_cmp_le_u64_e64 s[18:19], s[4:5], v[0:1]
	s_bcnt1_i32_b64 s5, s[18:19]
	s_cmp_gt_i32 s5, 15
	s_cselect_b32 s7, s4, s7
	s_cmp_eq_u32 s5, 16
	s_cbranch_scc1 .Ltopk_exit
	s_or_b32 s4, s7, 2
	s_mov_b32 s5, s1
	v_cmp_le_u64_e64 s[18:19], s[4:5], v[0:1]
	s_bcnt1_i32_b64 s5, s[18:19]
	s_cmp_gt_i32 s5, 15
	s_cselect_b32 s7, s4, s7
	s_cmp_eq_u32 s5, 16
	s_cbranch_scc1 .Ltopk_exit
	s_or_b32 s4, s7, 1
	s_mov_b32 s5, s1
	v_cmp_le_u64_e64 s[18:19], s[4:5], v[0:1]
	s_bcnt1_i32_b64 s5, s[18:19]
	s_cmp_gt_i32 s5, 15
	s_cselect_b32 s4, s4, s7
.Ltopk_fin:
	s_mov_b32 s5, s1
	s_mov_b32 s1, 0xf0c9f2ca
	v_cmp_le_u64_e64 s[18:19], s[4:5], v[0:1]
	v_cmp_lt_f32_e64 s[20:21], s1, v5
	s_and_b64 s[4:5], s[18:19], s[20:21]
	v_cndmask_b32_e64 v0, 0, 1, s[4:5]
	v_cmp_ne_u32_e64 s[18:19], 0, v0
	s_and_saveexec_b64 s[4:5], s[46:47]
	s_cbranch_execz .LBB0_1692
	s_add_i32 s1, s6, 0
	v_mov_b32_e32 v0, s1
	v_mov_b64_e32 v[6:7], s[18:19]
	s_waitcnt vmcnt(0)
	ds_write_b64 v0, v[6:7]
	s_branch .LBB0_1692
.Ltopk_exit:
	s_mov_b32 s4, s7
	s_branch .Ltopk_fin
